# sel: a block's next-triple DMA issue is interleaved into the PV MFMA stream of the tile executing in that block (issued at the block head only when the wave has no tile there)
# speedup vs baseline: 1.0024x; 1.0024x over previous
; #define LAS __attribute__((address_space(3)))
; #define RING_BARRIER() do { asm volatile("s_waitcnt lgkmcnt(0)" ::: "memory"); __builtin_amdgcn_s_barrier(); asm volatile("" ::: "memory"); } while (0)
; __device__ __forceinline__ void ringS_dma(const RingSLane& R, const char* K8p, const char* VTp, LAS unsigned char* sb, int wave) {
;     __builtin_amdgcn_global_load_lds((const unsigned*)(K8p + R.so[0]), (LAS unsigned*)(sb + wave * 1024), 16, 0, 0);
;     __builtin_amdgcn_global_load_lds((const unsigned*)((wave == 0 ? K8p : VTp) + R.so[1]), (LAS unsigned*)(sb + (wave + 8) * 1024), 16, 0, 0);
;     if (wave <= 2) __builtin_amdgcn_global_load_lds((const unsigned*)(VTp + R.so[2]), (LAS unsigned*)(sb + (wave + 16) * 1024), 16, 0, 0);
; }
; template <bool DUMMY> __device__ __forceinline__ void sel_phase(Frame& F) {
;     ...
;         for (int p = 0; p < npair; ++p) {
;             u32x2 dnx = {0xffffffffu, 0u}; if (p + 1 < npair) dnx = PD[(p + 1) * 8 + F.wave];
;             asm volatile("s_waitcnt vmcnt(0)" ::: "memory"); RING_BARRIER();
;             const unsigned nj = (unsigned)__builtin_amdgcn_readfirstlane((int)dnx.x), nb = (unsigned)__builtin_amdgcn_readfirstlane((int)dnx.y);
;             if (p + 1 < npair && !(DUMMY && MK_EXP == 2)) { SEL_DMA3(nj, F.lds + ((p + 1) & 1) * 3 * SLOTS); }
; #pragma unroll 1
;             for (int h = 0; h < 3; ++h) {
;                 if (h > 0 && ((cj >> (23 + h)) & 1u) == 0u) continue;
;                 const int jc = (int)((cj >> (8 * h)) & 0xffu);
;                 LAS unsigned char* sb = F.lds + (((p & 1) * 3) + h) * SLOTS;
;                 unsigned byte = (cb >> (8 * h)) & 0xffu;
;                 if (DUMMY && MK_EXP == 1) byte = 0u;
;                 const unsigned a0 = byte & 0xfu, a1 = byte >> 4;
;                 if (byte == 0u) continue;
.LBB0_1799:
	s_lshr_b32 s45, s67, s36
	s_and_b32 s97, s45, 0xff
	s_cbranch_scc1 .Lsel_tile
	s_bitcmp1_b32 s99, s37
	s_cbranch_scc0 .LBB0_1798
	s_lshr_b32 s12, s60, s36
	s_and_b32 s12, s12, 0xff
	s_lshl_b32 s12, s12, 13
	s_add_u32 s44, s62, s12
	s_addc_u32 s45, s63, 0
	s_add_u32 s12, s64, s12
	s_addc_u32 s13, s65, 0
	s_mul_i32 s97, s37, 0x4c00
	s_add_i32 s97, s98, s97
	s_mov_b32 m0, s97
	s_and_b64 vcc, exec, s[16:17]
	global_load_lds_dwordx4 v102, s[44:45]
	s_cselect_b32 s45, s45, s13
	s_cselect_b32 s44, s44, s12
	s_add_i32 m0, s97, 0x2000
	s_and_b64 vcc, exec, s[10:11]
	global_load_lds_dwordx4 v106, s[44:45]
	s_cbranch_vccnz .LBB0_1798
	s_add_i32 m0, s97, 0x4000
	s_nop 0
	global_load_lds_dwordx4 v108, s[12:13]
	s_branch .LBB0_1798
.Lsel_tile:
	ds_read_b128 v[84:87], v208 offset:0
	ds_read_b128 v[88:91], v208 offset:16
	ds_read_b128 v[92:95], v208 offset:0x900
	ds_read_b128 v[96:99], v208 offset:0x910
	ds_read_b128 v[118:121], v208 offset:0x1200
	ds_read_b128 v[122:125], v208 offset:0x1210
	s_and_b32 vcc_lo, s45, 15
	s_cbranch_scc0 .Lsel_g1_pre
	v_and_b32_e32 v18, s45, v154
	v_cmp_eq_u32_e32 vcc, 0, v18
	s_lshr_b32 s44, s66, s36
	s_and_b32 s44, s44, 0xff
	v_cndmask_b32_e32 v210, v216, v181, vcc
	v_mov_b32_e32 v211, v210
	v_mov_b32_e32 v212, v210
	v_mov_b32_e32 v213, v210
	ds_read_b128 v[126:129], v208 offset:0x1b00
	ds_read_b128 v[130:133], v208 offset:0x1b10
	s_waitcnt lgkmcnt(6)
	v_mfma_scale_f32_16x16x128_f8f6f4 v[84:87], v[84:91], v[0:7], v[210:213], v178, v177 op_sel_hi:[0,0,0]
	ds_read_b128 v[134:137], v207 offset:0
	ds_read_b128 v[138:141], v207 offset:0x500
	ds_read_b128 v[142:145], v207 offset:0xa00
	ds_read_b128 v[146:149], v207 offset:0xf00
	s_waitcnt lgkmcnt(8)
	v_mfma_scale_f32_16x16x128_f8f6f4 v[88:91], v[92:99], v[0:7], v[210:213], v178, v177 op_sel_hi:[0,0,0]
	s_waitcnt lgkmcnt(6)
	v_mfma_scale_f32_16x16x128_f8f6f4 v[92:95], v[118:125], v[0:7], v[210:213], v178, v177 op_sel_hi:[0,0,0]
	s_waitcnt lgkmcnt(4)
	v_mfma_scale_f32_16x16x128_f8f6f4 v[96:99], v[126:133], v[0:7], v[210:213], v178, v177 op_sel_hi:[0,0,0]
	ds_read_b128 v[118:121], v207 offset:0x1400
	ds_read_b128 v[122:125], v207 offset:0x1900
	ds_read_b128 v[126:129], v207 offset:0x1e00
	ds_read_b128 v[130:133], v207 offset:0x2300
	s_cmp_eq_u32 s44, s58
	s_cbranch_scc1 .Lsel_diag_g0

; __device__ __forceinline__ unsigned pk4_fp8(float a, float b, float c, float d) { unsigned w = 0u; w = __builtin_amdgcn_cvt_pk_fp8_f32(a, b, w, false); w = __builtin_amdgcn_cvt_pk_fp8_f32(c, d, w, true); return w; }
; #define LGKM_W(n) asm volatile("s_waitcnt lgkmcnt(" #n ")" ::: "memory"); SBAR()
; #define PV8_MM(dt) do { g.o[dt] = __builtin_amdgcn_mfma_f32_16x16x32_fp8_fp8(f.a[dt][0], b0, g.o[dt], 0, 0, 0); g.o[dt] = __builtin_amdgcn_mfma_f32_16x16x32_fp8_fp8(f.a[dt][1], b1, g.o[dt], 0, 0, 0); } while (0)
; template <class G> __device__ __forceinline__ void pv8_mm(G& g, const f32x4 (&s)[4], const VT8Frag& f) {
;     ...
;     unsigned pa[4];
; #pragma unroll
;     for (int T_ = 0; T_ < 4; ++T_) pa[T_] = pk4_fp8(s[T_][0], s[T_][1], s[T_][2], s[T_][3]);
;     const long b0 = (long)(((unsigned long long)pa[1] << 32) | pa[0]), b1 = (long)(((unsigned long long)pa[3] << 32) | pa[2]);
;     LGKM_W(14); PV8_MM(0); LGKM_W(12); PV8_MM(1); LGKM_W(10); PV8_MM(2); LGKM_W(8); PV8_MM(3);
;     LGKM_W(6); PV8_MM(4); LGKM_W(4); PV8_MM(5); LGKM_W(2); PV8_MM(6); LGKM_W(0); PV8_MM(7);
; template <class G> __device__ __forceinline__ void online_sm8(f32x4 (&s)[4], G& g, const float ref) {
;     ...
;     float ps = 0.f;
; #pragma unroll
;     for (int T_ = 0; T_ < 4; ++T_)
; #pragma unroll
;         for (int i = 0; i < 4; ++i) { s[T_][i] = __builtin_amdgcn_exp2f(s[T_][i]); ps += s[T_][i]; }
;     g.l += ps;
.LBB0_1808:
	v_exp_f32_e32 v240, v84
	v_exp_f32_e32 v241, v85
	v_exp_f32_e32 v242, v86
	v_exp_f32_e32 v243, v87
	v_exp_f32_e32 v244, v88
	v_exp_f32_e32 v245, v89
	v_exp_f32_e32 v246, v90
	v_exp_f32_e32 v247, v91
	s_waitcnt lgkmcnt(0)
	v_cvt_pk_fp8_f32 v84, v240, v241
	v_cvt_pk_fp8_f32 v85, v244, v245
	v_cvt_pk_fp8_f32 v84, v242, v243 op_sel:[0,0,1]
	v_cvt_pk_fp8_f32 v85, v246, v247 op_sel:[0,0,1]
	v_exp_f32_e32 v248, v92
	v_exp_f32_e32 v249, v93
	v_mfma_f32_16x16x32_fp8_fp8 v[80:83], v[134:135], v[84:85], v[80:83]
	v_exp_f32_e32 v250, v94
	v_mfma_f32_16x16x32_fp8_fp8 v[76:79], v[138:139], v[84:85], v[76:79]
	v_exp_f32_e32 v251, v95
	v_mfma_f32_16x16x32_fp8_fp8 v[72:75], v[142:143], v[84:85], v[72:75]
	v_exp_f32_e32 v252, v96
	v_mfma_f32_16x16x32_fp8_fp8 v[68:71], v[146:147], v[84:85], v[68:71]
	v_exp_f32_e32 v253, v97
	v_mfma_f32_16x16x32_fp8_fp8 v[64:67], v[118:119], v[84:85], v[64:67]
	v_exp_f32_e32 v254, v98
	v_mfma_f32_16x16x32_fp8_fp8 v[60:63], v[122:123], v[84:85], v[60:63]
	v_exp_f32_e32 v255, v99
	v_mfma_f32_16x16x32_fp8_fp8 v[56:59], v[126:127], v[84:85], v[56:59]
	v_mfma_f32_16x16x32_fp8_fp8 v[52:55], v[130:131], v[84:85], v[52:55]
	s_bitcmp1_b32 s99, s37
	s_cbranch_scc1 .Lsel_pd_dma_g0
	v_cvt_pk_fp8_f32 v86, v248, v249
	v_cvt_pk_fp8_f32 v87, v252, v253
	v_cvt_pk_fp8_f32 v86, v250, v251 op_sel:[0,0,1]
	v_cvt_pk_fp8_f32 v87, v254, v255 op_sel:[0,0,1]
	v_add_f32_e32 v240, v240, v241
	v_add_f32_e32 v242, v242, v243
	v_mfma_f32_16x16x32_fp8_fp8 v[80:83], v[136:137], v[86:87], v[80:83]
	v_add_f32_e32 v244, v244, v245
	v_add_f32_e32 v246, v246, v247
	v_mfma_f32_16x16x32_fp8_fp8 v[76:79], v[140:141], v[86:87], v[76:79]
	v_add_f32_e32 v248, v248, v249
	v_add_f32_e32 v250, v250, v251
	v_mfma_f32_16x16x32_fp8_fp8 v[72:75], v[144:145], v[86:87], v[72:75]
	v_add_f32_e32 v252, v252, v253
	v_add_f32_e32 v254, v254, v255
	v_mfma_f32_16x16x32_fp8_fp8 v[68:71], v[148:149], v[86:87], v[68:71]
	v_add_f32_e32 v240, v240, v242
	v_add_f32_e32 v244, v244, v246
	v_mfma_f32_16x16x32_fp8_fp8 v[64:67], v[120:121], v[86:87], v[64:67]
	v_add_f32_e32 v248, v248, v250
	v_add_f32_e32 v252, v252, v254
	v_mfma_f32_16x16x32_fp8_fp8 v[60:63], v[124:125], v[86:87], v[60:63]
	v_add_f32_e32 v240, v240, v244
	v_add_f32_e32 v248, v248, v252
	v_mfma_f32_16x16x32_fp8_fp8 v[56:59], v[128:129], v[86:87], v[56:59]
	v_add_f32_e32 v240, v240, v248
	v_add_f32_e32 v183, v183, v240
	v_mfma_f32_16x16x32_fp8_fp8 v[52:55], v[132:133], v[86:87], v[52:55]

; #define LAS __attribute__((address_space(3)))
; __device__ __forceinline__ unsigned pk4_fp8(float a, float b, float c, float d) { unsigned w = 0u; w = __builtin_amdgcn_cvt_pk_fp8_f32(a, b, w, false); w = __builtin_amdgcn_cvt_pk_fp8_f32(c, d, w, true); return w; }
; #define LGKM_W(n) asm volatile("s_waitcnt lgkmcnt(" #n ")" ::: "memory"); SBAR()
; #define PV8_MM(dt) do { g.o[dt] = __builtin_amdgcn_mfma_f32_16x16x32_fp8_fp8(f.a[dt][0], b0, g.o[dt], 0, 0, 0); g.o[dt] = __builtin_amdgcn_mfma_f32_16x16x32_fp8_fp8(f.a[dt][1], b1, g.o[dt], 0, 0, 0); } while (0)
; __device__ __forceinline__ void ringS_dma(const RingSLane& R, const char* K8p, const char* VTp, LAS unsigned char* sb, int wave) {
;     __builtin_amdgcn_global_load_lds((const unsigned*)(K8p + R.so[0]), (LAS unsigned*)(sb + wave * 1024), 16, 0, 0);
;     __builtin_amdgcn_global_load_lds((const unsigned*)((wave == 0 ? K8p : VTp) + R.so[1]), (LAS unsigned*)(sb + (wave + 8) * 1024), 16, 0, 0);
;     if (wave <= 2) __builtin_amdgcn_global_load_lds((const unsigned*)(VTp + R.so[2]), (LAS unsigned*)(sb + (wave + 16) * 1024), 16, 0, 0);
; }
; template <class G> __device__ __forceinline__ void pv8_mm(G& g, const f32x4 (&s)[4], const VT8Frag& f) {
;     ...
;     unsigned pa[4];
; #pragma unroll
;     for (int T_ = 0; T_ < 4; ++T_) pa[T_] = pk4_fp8(s[T_][0], s[T_][1], s[T_][2], s[T_][3]);
;     const long b0 = (long)(((unsigned long long)pa[1] << 32) | pa[0]), b1 = (long)(((unsigned long long)pa[3] << 32) | pa[2]);
;     LGKM_W(14); PV8_MM(0); LGKM_W(12); PV8_MM(1); LGKM_W(10); PV8_MM(2); LGKM_W(8); PV8_MM(3);
;     LGKM_W(6); PV8_MM(4); LGKM_W(4); PV8_MM(5); LGKM_W(2); PV8_MM(6); LGKM_W(0); PV8_MM(7);
.LBB0_1797:
	v_exp_f32_e32 v240, v84
	v_exp_f32_e32 v241, v85
	v_exp_f32_e32 v242, v86
	v_exp_f32_e32 v243, v87
	v_exp_f32_e32 v244, v88
	v_exp_f32_e32 v245, v89
	v_exp_f32_e32 v246, v90
	v_exp_f32_e32 v247, v91
	s_waitcnt lgkmcnt(0)
	v_cvt_pk_fp8_f32 v84, v240, v241
	v_cvt_pk_fp8_f32 v85, v244, v245
	v_cvt_pk_fp8_f32 v84, v242, v243 op_sel:[0,0,1]
	v_cvt_pk_fp8_f32 v85, v246, v247 op_sel:[0,0,1]
	v_exp_f32_e32 v248, v92
	v_exp_f32_e32 v249, v93
	v_mfma_f32_16x16x32_fp8_fp8 v[48:51], v[134:135], v[84:85], v[48:51]
	v_exp_f32_e32 v250, v94
	v_mfma_f32_16x16x32_fp8_fp8 v[44:47], v[138:139], v[84:85], v[44:47]
	v_exp_f32_e32 v251, v95
	v_mfma_f32_16x16x32_fp8_fp8 v[40:43], v[142:143], v[84:85], v[40:43]
	v_exp_f32_e32 v252, v96
	v_mfma_f32_16x16x32_fp8_fp8 v[36:39], v[146:147], v[84:85], v[36:39]
	v_exp_f32_e32 v253, v97
	v_mfma_f32_16x16x32_fp8_fp8 v[32:35], v[118:119], v[84:85], v[32:35]
	v_exp_f32_e32 v254, v98
	v_mfma_f32_16x16x32_fp8_fp8 v[28:31], v[122:123], v[84:85], v[28:31]
	v_exp_f32_e32 v255, v99
	v_mfma_f32_16x16x32_fp8_fp8 v[24:27], v[126:127], v[84:85], v[24:27]
	v_mfma_f32_16x16x32_fp8_fp8 v[20:23], v[130:131], v[84:85], v[20:23]
	s_bitcmp1_b32 s99, s37
	s_cbranch_scc1 .Lsel_pd_dma_g1
	v_cvt_pk_fp8_f32 v86, v248, v249
	v_cvt_pk_fp8_f32 v87, v252, v253
	v_cvt_pk_fp8_f32 v86, v250, v251 op_sel:[0,0,1]
	v_cvt_pk_fp8_f32 v87, v254, v255 op_sel:[0,0,1]
	v_add_f32_e32 v240, v240, v241
	v_add_f32_e32 v242, v242, v243
	v_mfma_f32_16x16x32_fp8_fp8 v[48:51], v[136:137], v[86:87], v[48:51]
	v_add_f32_e32 v244, v244, v245
	v_add_f32_e32 v246, v246, v247
	v_mfma_f32_16x16x32_fp8_fp8 v[44:47], v[140:141], v[86:87], v[44:47]
	v_add_f32_e32 v248, v248, v249
	v_add_f32_e32 v250, v250, v251
	v_mfma_f32_16x16x32_fp8_fp8 v[40:43], v[144:145], v[86:87], v[40:43]
	v_add_f32_e32 v252, v252, v253
	v_add_f32_e32 v254, v254, v255
	v_mfma_f32_16x16x32_fp8_fp8 v[36:39], v[148:149], v[86:87], v[36:39]
	v_add_f32_e32 v240, v240, v242
	v_add_f32_e32 v244, v244, v246
	v_mfma_f32_16x16x32_fp8_fp8 v[32:35], v[120:121], v[86:87], v[32:35]
	v_add_f32_e32 v248, v248, v250
	v_add_f32_e32 v252, v252, v254
	v_mfma_f32_16x16x32_fp8_fp8 v[28:31], v[124:125], v[86:87], v[28:31]
	v_add_f32_e32 v240, v240, v244
	v_add_f32_e32 v248, v248, v252
	v_mfma_f32_16x16x32_fp8_fp8 v[24:27], v[128:129], v[86:87], v[24:27]
	v_add_f32_e32 v240, v240, v248
	v_add_f32_e32 v182, v182, v240
	v_mfma_f32_16x16x32_fp8_fp8 v[20:23], v[132:133], v[86:87], v[20:23]
	s_branch .LBB0_1798
.Lsel_pd_dma_g0:
	v_cvt_pk_fp8_f32 v86, v248, v249
	v_cvt_pk_fp8_f32 v87, v252, v253
	v_cvt_pk_fp8_f32 v86, v250, v251 op_sel:[0,0,1]
	v_cvt_pk_fp8_f32 v87, v254, v255 op_sel:[0,0,1]
	v_add_f32_e32 v240, v240, v241
	v_add_f32_e32 v242, v242, v243
	v_mfma_f32_16x16x32_fp8_fp8 v[80:83], v[136:137], v[86:87], v[80:83]
	s_lshr_b32 vcc_lo, s60, s36
	s_and_b32 vcc_lo, vcc_lo, 0xff
	s_lshl_b32 vcc_lo, vcc_lo, 13
	v_add_f32_e32 v244, v244, v245
	v_add_f32_e32 v246, v246, v247
	v_mfma_f32_16x16x32_fp8_fp8 v[76:79], v[140:141], v[86:87], v[76:79]
	s_add_u32 s12, s62, vcc_lo
	s_addc_u32 s13, s63, 0
	s_add_u32 s100, s64, vcc_lo
	v_add_f32_e32 v248, v248, v249
	v_add_f32_e32 v250, v250, v251
	v_mfma_f32_16x16x32_fp8_fp8 v[72:75], v[144:145], v[86:87], v[72:75]
	s_addc_u32 s101, s65, 0
	s_mul_i32 vcc_hi, s37, 0x4c00
	s_add_i32 vcc_hi, s98, vcc_hi
	v_add_f32_e32 v252, v252, v253
	v_add_f32_e32 v254, v254, v255
	v_mfma_f32_16x16x32_fp8_fp8 v[68:71], v[148:149], v[86:87], v[68:71]
	s_mov_b32 m0, vcc_hi
	s_cmp_lg_u64 s[16:17], 0
	global_load_lds_dwordx4 v102, s[12:13]
	v_add_f32_e32 v240, v240, v242
	v_add_f32_e32 v244, v244, v246
	v_mfma_f32_16x16x32_fp8_fp8 v[64:67], v[120:121], v[86:87], v[64:67]
	s_cselect_b32 s13, s13, s101
	s_cselect_b32 s12, s12, s100
	v_add_f32_e32 v248, v248, v250
	v_add_f32_e32 v252, v252, v254
	v_mfma_f32_16x16x32_fp8_fp8 v[60:63], v[124:125], v[86:87], v[60:63]
	s_add_i32 m0, vcc_hi, 0x2000
	s_cmp_lg_u64 s[10:11], 0
	v_add_f32_e32 v240, v240, v244
	v_add_f32_e32 v248, v248, v252
	v_mfma_f32_16x16x32_fp8_fp8 v[56:59], v[128:129], v[86:87], v[56:59]
	global_load_lds_dwordx4 v106, s[12:13]
	s_bitset0_b32 s99, s37
	v_add_f32_e32 v240, v240, v248
	v_add_f32_e32 v183, v183, v240
	v_mfma_f32_16x16x32_fp8_fp8 v[52:55], v[132:133], v[86:87], v[52:55]
	s_cbranch_scc1 .Lsel_pd_end_g0
	s_add_i32 m0, vcc_hi, 0x4000
	s_nop 0
	global_load_lds_dwordx4 v108, s[100:101]

; #define LAS __attribute__((address_space(3)))
; __device__ __forceinline__ void mask_scores(f32x4 (&s)[4], int a, unsigned W, int kb, int q4) {
;     const float NEG = -__builtin_inff();
; #pragma unroll
;     for (int T_ = 0; T_ < 4; ++T_)
; #pragma unroll
;         for (int i = 0; i < 4; ++i) if ((unsigned)(a - (kb + 16 * T_ + 4 * q4 + i)) >= W) s[T_][i] = NEG;
; }
; __device__ __forceinline__ void ringS_dma(const RingSLane& R, const char* K8p, const char* VTp, LAS unsigned char* sb, int wave) {
;     __builtin_amdgcn_global_load_lds((const unsigned*)(K8p + R.so[0]), (LAS unsigned*)(sb + wave * 1024), 16, 0, 0);
;     __builtin_amdgcn_global_load_lds((const unsigned*)((wave == 0 ? K8p : VTp) + R.so[1]), (LAS unsigned*)(sb + (wave + 8) * 1024), 16, 0, 0);
;     if (wave <= 2) __builtin_amdgcn_global_load_lds((const unsigned*)(VTp + R.so[2]), (LAS unsigned*)(sb + (wave + 16) * 1024), 16, 0, 0);
; }
.Lsel_pd_dma_g1:
	v_cvt_pk_fp8_f32 v86, v248, v249
	v_cvt_pk_fp8_f32 v87, v252, v253
	v_cvt_pk_fp8_f32 v86, v250, v251 op_sel:[0,0,1]
	v_cvt_pk_fp8_f32 v87, v254, v255 op_sel:[0,0,1]
	v_add_f32_e32 v240, v240, v241
	v_add_f32_e32 v242, v242, v243
	v_mfma_f32_16x16x32_fp8_fp8 v[48:51], v[136:137], v[86:87], v[48:51]
	s_lshr_b32 vcc_lo, s60, s36
	s_and_b32 vcc_lo, vcc_lo, 0xff
	s_lshl_b32 vcc_lo, vcc_lo, 13
	v_add_f32_e32 v244, v244, v245
	v_add_f32_e32 v246, v246, v247
	v_mfma_f32_16x16x32_fp8_fp8 v[44:47], v[140:141], v[86:87], v[44:47]
	s_add_u32 s12, s62, vcc_lo
	s_addc_u32 s13, s63, 0
	s_add_u32 s100, s64, vcc_lo
	v_add_f32_e32 v248, v248, v249
	v_add_f32_e32 v250, v250, v251
	v_mfma_f32_16x16x32_fp8_fp8 v[40:43], v[144:145], v[86:87], v[40:43]
	s_addc_u32 s101, s65, 0
	s_mul_i32 vcc_hi, s37, 0x4c00
	s_add_i32 vcc_hi, s98, vcc_hi
	v_add_f32_e32 v252, v252, v253
	v_add_f32_e32 v254, v254, v255
	v_mfma_f32_16x16x32_fp8_fp8 v[36:39], v[148:149], v[86:87], v[36:39]
	s_mov_b32 m0, vcc_hi
	s_cmp_lg_u64 s[16:17], 0
	global_load_lds_dwordx4 v102, s[12:13]
	v_add_f32_e32 v240, v240, v242
	v_add_f32_e32 v244, v244, v246
	v_mfma_f32_16x16x32_fp8_fp8 v[32:35], v[120:121], v[86:87], v[32:35]
	s_cselect_b32 s13, s13, s101
	s_cselect_b32 s12, s12, s100
	v_add_f32_e32 v248, v248, v250
	v_add_f32_e32 v252, v252, v254
	v_mfma_f32_16x16x32_fp8_fp8 v[28:31], v[124:125], v[86:87], v[28:31]
	s_add_i32 m0, vcc_hi, 0x2000
	s_cmp_lg_u64 s[10:11], 0
	v_add_f32_e32 v240, v240, v244
	v_add_f32_e32 v248, v248, v252
	v_mfma_f32_16x16x32_fp8_fp8 v[24:27], v[128:129], v[86:87], v[24:27]
	global_load_lds_dwordx4 v106, s[12:13]
	s_bitset0_b32 s99, s37
	v_add_f32_e32 v240, v240, v248
	v_add_f32_e32 v182, v182, v240
	v_mfma_f32_16x16x32_fp8_fp8 v[20:23], v[132:133], v[86:87], v[20:23]
	s_cbranch_scc1 .Lsel_pd_end_g1
	s_add_i32 m0, vcc_hi, 0x4000
	s_nop 0
	global_load_lds_dwordx4 v108, s[100:101]
.Lsel_pd_end_g1:
	s_branch .LBB0_1798
.Lsel_diag_g0:
	s_lshl_b32 s12, s44, 6
	v_add_u32_e32 v18, s12, v155
	v_sub_u32_e32 v114, s55, v18
	v_cmp_gt_u32_e32 vcc, 2.0, v114
	v_sub_u32_e32 v114, v18, v16
	s_nop 2
	v_cndmask_b32_e32 v84, v181, v84, vcc
	v_cmp_lt_u32_e32 vcc, s91, v114
	v_sub_u32_e32 v114, v184, v18
	s_nop 0
	v_cndmask_b32_e32 v85, v181, v85, vcc
	v_cmp_gt_u32_e32 vcc, 2.0, v114
	v_sub_u32_e32 v114, v185, v18
	s_nop 0
	v_cndmask_b32_e32 v86, v181, v86, vcc
	v_cmp_gt_u32_e32 vcc, 2.0, v114
	v_sub_u32_e32 v114, s68, v18
	s_nop 0
	v_cndmask_b32_e32 v87, v181, v87, vcc
	v_cmp_gt_u32_e32 vcc, 2.0, v114
	v_sub_u32_e32 v114, v186, v18
	s_nop 0
	v_cndmask_b32_e32 v88, v181, v88, vcc
	v_cmp_gt_u32_e32 vcc, 2.0, v114
	v_sub_u32_e32 v114, v187, v18
	s_nop 0
	v_cndmask_b32_e32 v89, v181, v89, vcc
	v_cmp_gt_u32_e32 vcc, 2.0, v114
	v_sub_u32_e32 v114, v188, v18
	s_nop 0
	v_cndmask_b32_e32 v90, v181, v90, vcc
	v_cmp_gt_u32_e32 vcc, 2.0, v114
	v_sub_u32_e32 v114, s69, v18
	s_nop 0
	v_cndmask_b32_e32 v91, v181, v91, vcc
	v_cmp_gt_u32_e32 vcc, 2.0, v114
	v_sub_u32_e32 v114, v189, v18
	s_nop 0
	v_cndmask_b32_e32 v92, v181, v92, vcc
	v_cmp_gt_u32_e32 vcc, 2.0, v114
	v_sub_u32_e32 v114, v190, v18
	s_nop 0
	v_cndmask_b32_e32 v93, v181, v93, vcc
	v_cmp_gt_u32_e32 vcc, 2.0, v114
	v_sub_u32_e32 v114, v191, v18
	s_nop 0
	v_cndmask_b32_e32 v94, v181, v94, vcc
	v_cmp_gt_u32_e32 vcc, 2.0, v114
	v_sub_u32_e32 v114, s70, v18
	s_nop 0
	v_cndmask_b32_e32 v95, v181, v95, vcc
	v_cmp_gt_u32_e32 vcc, 2.0, v114
	v_sub_u32_e32 v114, v192, v18
	s_nop 0
	v_cndmask_b32_e32 v96, v181, v96, vcc
	v_cmp_gt_u32_e32 vcc, 2.0, v114
	v_sub_u32_e32 v114, v193, v18
	v_sub_u32_e32 v18, v194, v18
	v_cndmask_b32_e32 v97, v181, v97, vcc
	v_cmp_gt_u32_e32 vcc, 2.0, v114
	s_nop 1
	v_cndmask_b32_e32 v98, v181, v98, vcc
	v_cmp_gt_u32_e32 vcc, 2.0, v18
	s_nop 1
	v_cndmask_b32_e32 v99, v181, v99, vcc
	s_branch .LBB0_1806
